# baseline (speedup 1.0000x reference)
_Z8knn_gemmPKcS0_Pi:
	s_ashr_i32 s3, s2, 31
	s_lshr_b32 s3, s3, 29
	s_add_i32 s3, s2, s3
	s_ashr_i32 s4, s3, 3
	s_and_b32 s3, s3, -8
	s_sub_i32 s3, s2, s3
	s_cmp_lt_i32 s3, 0
	s_movk_i32 s12, 0x188
	s_cselect_b32 s5, s12, 0x187
	s_mul_i32 s3, s5, s3
	s_add_i32 s3, s3, s4
	s_ashr_i32 s4, s3, 31
	s_lshr_b32 s4, s4, 27
	s_add_i32 s10, s3, s4
	s_ashr_i32 s4, s10, 5
	s_lshl_b32 s11, s4, 2
	s_sub_i32 s4, 0x187, s11
	s_min_i32 s13, s4, 4
	s_abs_i32 s14, s13
	v_cvt_f32_u32_e32 v1, s14
	s_andn2_b32 s10, s10, 31
	s_load_dwordx4 s[4:7], s[0:1], 0x0
	s_load_dwordx2 s[8:9], s[0:1], 0x10
	s_sub_i32 s0, s3, s10
	v_rcp_iflag_f32_e32 v1, v1
	s_sub_i32 s10, 0, s14
	s_abs_i32 s3, s0
	s_xor_b32 s1, s0, s13
	v_mul_f32_e32 v1, 0x4f7ffffe, v1
	v_cvt_u32_f32_e32 v1, v1
	s_ashr_i32 s1, s1, 31
	v_lshrrev_b32_e32 v2, 8, v0
	v_lshlrev_b32_e32 v168, 4, v0
	v_readfirstlane_b32 s15, v1
	s_mul_i32 s10, s10, s15
	s_mul_hi_u32 s10, s15, s10
	s_add_i32 s15, s15, s10
	s_mul_hi_u32 s10, s3, s15
	s_mul_i32 s15, s10, s14
	s_sub_i32 s3, s3, s15
	s_add_i32 s15, s10, 1
	s_sub_i32 s16, s3, s14
	s_cmp_ge_u32 s3, s14
	s_cselect_b32 s10, s15, s10
	s_cselect_b32 s3, s16, s3
	s_add_i32 s15, s10, 1
	s_cmp_ge_u32 s3, s14
	s_cselect_b32 s3, s15, s10
	s_xor_b32 s3, s3, s1
	s_sub_i32 s34, s3, s1
	s_mul_i32 s1, s34, s13
	s_sub_i32 s0, s0, s1
	s_add_i32 s11, s11, s0
	v_readfirstlane_b32 s1, v0
	s_sub_i32 s13, 0x186, s11
	s_lshl_b32 s3, s1, 4
	s_mul_i32 s10, s34, 0x30000
	s_mul_hi_i32 s1, s34, 0x30000
	s_waitcnt lgkmcnt(0)
	s_add_u32 s10, s6, s10
	s_addc_u32 s11, s7, s1
	s_mul_i32 s14, s13, 0x30000
	s_mul_hi_i32 s1, s13, 0x30000
	s_add_u32 s22, s4, s14
	v_readfirstlane_b32 s0, v2
	s_addc_u32 s23, s5, s1
	s_cmp_eq_u32 s0, 0
	s_cselect_b64 s[0:1], -1, 0
	s_add_u32 s16, s10, 0x2000
	s_addc_u32 s17, s11, 0
	s_add_u32 s18, s22, 0xfffff000
	s_addc_u32 s19, s23, -1
	s_and_b64 s[14:15], s[0:1], exec
	s_cselect_b32 s17, s17, s19
	s_cselect_b32 s16, s16, s18
	s_add_u32 s18, s22, 0x1000
	s_addc_u32 s19, s23, 0
	s_add_i32 s14, s3, 0
	s_mov_b64 s[20:21], s[10:11]
	s_mov_b32 m0, s14
	s_add_i32 s15, s14, 0x2000
	v_lshrrev_b32_e32 v5, 2, v0
	global_load_lds_dwordx4 v168, s[20:21]
	s_mov_b32 m0, s15
	v_lshrrev_b32_e32 v1, 4, v0
	global_load_lds_dwordx4 v168, s[16:17]
	s_add_i32 s16, s14, 0x4000
	s_mov_b32 m0, s16
	v_and_b32_e32 v5, 2, v5
	global_load_lds_dwordx4 v168, s[18:19]
	s_add_u32 s18, s10, 0x3000
	s_addc_u32 s19, s11, 0
	s_add_u32 s3, s10, 0x5000
	s_addc_u32 s17, s11, 0
	s_add_u32 s20, s22, 0x2000
	s_addc_u32 s21, s23, 0
	s_and_b64 s[10:11], s[0:1], exec
	s_cselect_b32 s11, s17, s21
	s_cselect_b32 s10, s3, s20
	s_add_u32 s20, s22, 0x4000
	s_addc_u32 s21, s23, 0
	s_add_i32 s17, s14, 0x6000
	s_mov_b32 m0, s17
	v_add_lshl_u32 v1, v5, v1, 3
	global_load_lds_dwordx4 v168, s[18:19]
	s_add_i32 s18, s14, 0x8000
	s_mov_b32 m0, s18
	s_add_i32 s19, s14, 0xa000
	global_load_lds_dwordx4 v168, s[10:11]
	s_mov_b32 m0, s19
	v_and_b32_e32 v3, 15, v0
	global_load_lds_dwordx4 v168, s[20:21]
	v_and_b32_e32 v5, 24, v1
	v_lshrrev_b32_e32 v1, 1, v0
	s_movk_i32 s3, 0x60
	s_add_i32 s20, s14, 0xc000
	v_and_or_b32 v1, v1, s3, v3
	v_lshl_or_b32 v2, v2, 6, v3
	s_add_u32 s21, s4, 0x12000
	v_and_b32_e32 v4, 48, v0
	v_mad_u32_u24 v6, v1, s3, 0
	v_mad_u32_u24 v2, v2, s3, 0
	s_addc_u32 s22, s5, 0
	v_add_u32_e32 v1, v6, v4
	v_add_u32_e32 v170, v2, v4
	v_add_u32_e32 v172, v6, v5
	v_add_u32_e32 v173, v2, v5
	v_mov_b32_e32 v39, 0
	s_add_u32 s23, s6, 0x12000
	v_add_u32_e32 v171, 0x3000, v170
	v_add_u32_e32 v174, 0x3040, v173
	v_mov_b32_e32 v169, v39
	v_add_u32_e32 v175, 0x12000, v1
	v_add_u32_e32 v176, 0x12040, v172
	v_add_u32_e32 v177, 0x15000, v170
	v_add_u32_e32 v178, 0x15040, v173
	v_add_u32_e32 v179, 0x12600, v1
	v_add_u32_e32 v180, 0x12640, v172
	v_add_u32_e32 v181, 0x15600, v170
	v_add_u32_e32 v182, 0x15640, v173
	v_add_u32_e32 v183, 0x15c00, v170
	v_add_u32_e32 v184, 0x15c40, v173
	v_add_u32_e32 v185, 0x16200, v170
	v_add_u32_e32 v186, 0x16240, v173
	s_addc_u32 s24, s7, 0
	v_mov_b32_e32 v187, 0x7f7f7f7f
	s_add_i32 s25, 0, 0x18000
	s_movk_i32 s26, 0xff80
	s_movk_i32 s27, 0x30e
	s_add_i32 s28, s14, 0xe000
	s_add_i32 s29, s20, 0x4000
	s_add_i32 s30, s14, 0x12000
	s_add_i32 s31, s14, 0x14000
	s_add_i32 s33, s14, 0x16000
	s_and_b64 vcc, s[0:1], exec
	s_cbranch_scc0 .Lprio_g1
	s_setprio 2
	s_branch .LBB1_2
.Lprio_g1:
	s_setprio 1
	s_branch .LBB1_2

.LBB1_3:
	ds_read_b128 v[188:191], v1 offset:24576
	ds_read_b64 v[192:193], v172 offset:24640
	ds_read_b128 v[194:197], v1 offset:26112
	ds_read_b64 v[198:199], v172 offset:26176
	ds_read_b128 v[200:203], v170 offset:36864
	ds_read_b64 v[204:205], v173 offset:36928
	ds_read_b128 v[206:209], v170 offset:38400
	ds_read_b64 v[210:211], v173 offset:38464
	ds_read_b128 v[212:215], v170 offset:39936
	ds_read_b64 v[216:217], v173 offset:40000
	ds_read_b128 v[218:221], v170 offset:41472
	ds_read_b64 v[222:223], v173 offset:41536
	v_mfma_scale_f32_16x16x128_f8f6f4 v[164:167], v[2:7], v[20:25], v[164:167], v187, v187 op_sel_hi:[0,0,0] cbsz:2 blgp:2
	v_mfma_scale_f32_16x16x128_f8f6f4 v[160:163], v[8:13], v[20:25], v[160:163], v187, v187 op_sel_hi:[0,0,0] cbsz:2 blgp:2
	v_mfma_scale_f32_16x16x128_f8f6f4 v[156:159], v[14:19], v[20:25], v[156:159], v187, v187 op_sel_hi:[0,0,0] cbsz:2 blgp:2
	v_mfma_scale_f32_16x16x128_f8f6f4 v[152:155], v[26:31], v[20:25], v[152:155], v187, v187 op_sel_hi:[0,0,0] cbsz:2 blgp:2
	v_mfma_scale_f32_16x16x128_f8f6f4 v[148:151], v[2:7], v[32:37], v[148:151], v187, v187 op_sel_hi:[0,0,0] cbsz:2 blgp:2
	v_mfma_scale_f32_16x16x128_f8f6f4 v[140:143], v[8:13], v[32:37], v[140:143], v187, v187 op_sel_hi:[0,0,0] cbsz:2 blgp:2
	v_mfma_scale_f32_16x16x128_f8f6f4 v[132:135], v[14:19], v[32:37], v[132:135], v187, v187 op_sel_hi:[0,0,0] cbsz:2 blgp:2
	v_mfma_scale_f32_16x16x128_f8f6f4 v[124:127], v[26:31], v[32:37], v[124:127], v187, v187 op_sel_hi:[0,0,0] cbsz:2 blgp:2
	s_add_u32 s38, s2, 0xffffa000
	s_addc_u32 s39, s3, -1
	s_add_u32 s37, s2, 0xffffc000
	s_addc_u32 s42, s3, -1
	s_add_u32 s43, s11, 0xffff9000
	s_addc_u32 s44, s35, -1
	s_and_b64 s[40:41], s[0:1], exec
	s_cselect_b32 s41, s42, s44
	s_cselect_b32 s40, s37, s43
	s_add_u32 s42, s11, 0xffffb000
	s_addc_u32 s43, s35, -1
	s_mov_b32 m0, s14
	s_waitcnt vmcnt(3)
	s_barrier
	s_nop 0
	v_lshl_add_u64 v[224:225], s[38:39], 0, v[168:169]
	global_load_lds_dwordx4 v[224:225], off
	v_lshl_add_u64 v[224:225], s[40:41], 0, v[168:169]
	s_mov_b32 m0, s15
	s_nop 0
	global_load_lds_dwordx4 v[224:225], off
	v_lshl_add_u64 v[224:225], s[42:43], 0, v[168:169]
	s_mov_b32 m0, s16
	s_nop 0
	global_load_lds_dwordx4 v[224:225], off
	s_waitcnt lgkmcnt(0)
	v_mfma_scale_f32_16x16x128_f8f6f4 v[112:115], v[2:7], v[188:193], v[112:115], v187, v187 op_sel_hi:[0,0,0] cbsz:2 blgp:2
	v_mfma_scale_f32_16x16x128_f8f6f4 v[100:103], v[8:13], v[188:193], v[100:103], v187, v187 op_sel_hi:[0,0,0] cbsz:2 blgp:2
	v_mfma_scale_f32_16x16x128_f8f6f4 v[92:95], v[14:19], v[188:193], v[92:95], v187, v187 op_sel_hi:[0,0,0] cbsz:2 blgp:2
	v_mfma_scale_f32_16x16x128_f8f6f4 v[88:91], v[26:31], v[188:193], v[88:91], v187, v187 op_sel_hi:[0,0,0] cbsz:2 blgp:2
	v_mfma_scale_f32_16x16x128_f8f6f4 v[84:87], v[2:7], v[194:199], v[84:87], v187, v187 op_sel_hi:[0,0,0] cbsz:2 blgp:2
	v_mfma_scale_f32_16x16x128_f8f6f4 v[76:79], v[8:13], v[194:199], v[76:79], v187, v187 op_sel_hi:[0,0,0] cbsz:2 blgp:2
	v_mfma_scale_f32_16x16x128_f8f6f4 v[68:71], v[14:19], v[194:199], v[68:71], v187, v187 op_sel_hi:[0,0,0] cbsz:2 blgp:2
	v_mfma_scale_f32_16x16x128_f8f6f4 v[60:63], v[26:31], v[194:199], v[60:63], v187, v187 op_sel_hi:[0,0,0] cbsz:2 blgp:2
	ds_read_b128 v[2:5], v170 offset:61440
	ds_read_b64 v[6:7], v173 offset:61504
	ds_read_b128 v[8:11], v170 offset:62976
	ds_read_b64 v[12:13], v173 offset:63040
	ds_read_b128 v[14:17], v170 offset:64512
	ds_read_b64 v[18:19], v173 offset:64576
	ds_read_b128 v[26:29], v171 offset:53760
	ds_read_b64 v[30:31], v174 offset:53760
	v_mfma_scale_f32_16x16x128_f8f6f4 v[144:147], v[200:205], v[20:25], v[144:147], v187, v187 op_sel_hi:[0,0,0] cbsz:2 blgp:2
	v_mfma_scale_f32_16x16x128_f8f6f4 v[136:139], v[206:211], v[20:25], v[136:139], v187, v187 op_sel_hi:[0,0,0] cbsz:2 blgp:2
	v_mfma_scale_f32_16x16x128_f8f6f4 v[128:131], v[212:217], v[20:25], v[128:131], v187, v187 op_sel_hi:[0,0,0] cbsz:2 blgp:2
	v_mfma_scale_f32_16x16x128_f8f6f4 v[120:123], v[218:223], v[20:25], v[120:123], v187, v187 op_sel_hi:[0,0,0] cbsz:2 blgp:2
	v_mfma_scale_f32_16x16x128_f8f6f4 v[116:119], v[200:205], v[32:37], v[116:119], v187, v187 op_sel_hi:[0,0,0] cbsz:2 blgp:2
	v_mfma_scale_f32_16x16x128_f8f6f4 v[108:111], v[206:211], v[32:37], v[108:111], v187, v187 op_sel_hi:[0,0,0] cbsz:2 blgp:2
	v_mfma_scale_f32_16x16x128_f8f6f4 v[104:107], v[212:217], v[32:37], v[104:107], v187, v187 op_sel_hi:[0,0,0] cbsz:2 blgp:2
	v_mfma_scale_f32_16x16x128_f8f6f4 v[96:99], v[218:223], v[32:37], v[96:99], v187, v187 op_sel_hi:[0,0,0] cbsz:2 blgp:2
	s_add_u32 s38, s2, 0xffffd000
	s_addc_u32 s39, s3, -1
	s_add_u32 s37, s2, 0xfffff000
	s_addc_u32 s42, s3, -1
	s_add_u32 s43, s11, 0xffffc000
	s_addc_u32 s44, s35, -1
	s_and_b64 s[40:41], s[0:1], exec
	s_cselect_b32 s41, s42, s44
	s_cselect_b32 s40, s37, s43
	s_add_u32 s42, s11, 0xffffe000
	s_addc_u32 s43, s35, -1
	s_mov_b32 m0, s17
	ds_read_b128 v[20:23], v1 offset:49152
	ds_read_b64 v[24:25], v172 offset:49216
	ds_read_b128 v[32:35], v1 offset:50688
	ds_read_b64 v[36:37], v172 offset:50752
	s_waitcnt vmcnt(3)
	s_barrier
	s_nop 0
	v_lshl_add_u64 v[224:225], s[38:39], 0, v[168:169]
	global_load_lds_dwordx4 v[224:225], off
	v_lshl_add_u64 v[224:225], s[40:41], 0, v[168:169]
	s_mov_b32 m0, s18
	s_nop 0
	global_load_lds_dwordx4 v[224:225], off
	v_lshl_add_u64 v[224:225], s[42:43], 0, v[168:169]
	s_mov_b32 m0, s19
	s_nop 0
	global_load_lds_dwordx4 v[224:225], off
	v_mfma_scale_f32_16x16x128_f8f6f4 v[80:83], v[200:205], v[188:193], v[80:83], v187, v187 op_sel_hi:[0,0,0] cbsz:2 blgp:2
	v_mfma_scale_f32_16x16x128_f8f6f4 v[72:75], v[206:211], v[188:193], v[72:75], v187, v187 op_sel_hi:[0,0,0] cbsz:2 blgp:2
	v_mfma_scale_f32_16x16x128_f8f6f4 v[64:67], v[212:217], v[188:193], v[64:67], v187, v187 op_sel_hi:[0,0,0] cbsz:2 blgp:2
	v_mfma_scale_f32_16x16x128_f8f6f4 v[56:59], v[218:223], v[188:193], v[56:59], v187, v187 op_sel_hi:[0,0,0] cbsz:2 blgp:2
	v_mfma_scale_f32_16x16x128_f8f6f4 v[52:55], v[200:205], v[194:199], v[52:55], v187, v187 op_sel_hi:[0,0,0] cbsz:2 blgp:2
	v_mfma_scale_f32_16x16x128_f8f6f4 v[224:227], v[206:211], v[194:199], v[48:51], v187, v187 op_sel_hi:[0,0,0] cbsz:2 blgp:2
	v_mfma_scale_f32_16x16x128_f8f6f4 v[212:215], v[212:217], v[194:199], v[44:47], v187, v187 op_sel_hi:[0,0,0] cbsz:2 blgp:2
	v_mfma_scale_f32_16x16x128_f8f6f4 v[216:219], v[218:223], v[194:199], v[40:43], v187, v187 op_sel_hi:[0,0,0] cbsz:2 blgp:2
	s_waitcnt lgkmcnt(0)
	s_nop 0
	ds_read_b128 v[40:43], v175
	ds_read_b64 v[44:45], v176
	ds_read_b128 v[188:191], v179
	ds_read_b64 v[192:193], v180
	ds_read_b128 v[46:49], v177
	ds_read_b64 v[50:51], v178
	ds_read_b128 v[194:197], v181
	ds_read_b64 v[198:199], v182
	ds_read_b128 v[200:203], v183
	ds_read_b64 v[204:205], v184
	ds_read_b128 v[206:209], v185
	ds_read_b64 v[210:211], v186
	v_mfma_scale_f32_16x16x128_f8f6f4 v[164:167], v[2:7], v[20:25], v[164:167], v187, v187 op_sel_hi:[0,0,0] cbsz:2 blgp:2
	v_mfma_scale_f32_16x16x128_f8f6f4 v[160:163], v[8:13], v[20:25], v[160:163], v187, v187 op_sel_hi:[0,0,0] cbsz:2 blgp:2
	v_mfma_scale_f32_16x16x128_f8f6f4 v[156:159], v[14:19], v[20:25], v[156:159], v187, v187 op_sel_hi:[0,0,0] cbsz:2 blgp:2
	v_mfma_scale_f32_16x16x128_f8f6f4 v[152:155], v[26:31], v[20:25], v[152:155], v187, v187 op_sel_hi:[0,0,0] cbsz:2 blgp:2
	v_mfma_scale_f32_16x16x128_f8f6f4 v[148:151], v[2:7], v[32:37], v[148:151], v187, v187 op_sel_hi:[0,0,0] cbsz:2 blgp:2
	v_mfma_scale_f32_16x16x128_f8f6f4 v[140:143], v[8:13], v[32:37], v[140:143], v187, v187 op_sel_hi:[0,0,0] cbsz:2 blgp:2
	v_mfma_scale_f32_16x16x128_f8f6f4 v[132:135], v[14:19], v[32:37], v[132:135], v187, v187 op_sel_hi:[0,0,0] cbsz:2 blgp:2
	v_mfma_scale_f32_16x16x128_f8f6f4 v[124:127], v[26:31], v[32:37], v[124:127], v187, v187 op_sel_hi:[0,0,0] cbsz:2 blgp:2
	s_add_u32 s37, s2, 0x2000
	s_addc_u32 s40, s3, 0
	s_add_u32 s41, s11, 0xfffff000
	s_addc_u32 s42, s35, -1
	s_and_b64 s[38:39], s[0:1], exec
	s_cselect_b32 s39, s40, s42
	s_cselect_b32 s38, s37, s41
	s_add_u32 s40, s11, 0x1000
	s_addc_u32 s41, s35, 0
	s_mov_b64 s[42:43], s[2:3]
	s_mov_b32 m0, s20
	s_waitcnt vmcnt(3)
	s_barrier
	s_nop 0
	v_lshl_add_u64 v[220:221], s[42:43], 0, v[168:169]
	global_load_lds_dwordx4 v[220:221], off
	v_lshl_add_u64 v[220:221], s[38:39], 0, v[168:169]
	s_mov_b32 m0, s28
	s_nop 0
	global_load_lds_dwordx4 v[220:221], off
	v_lshl_add_u64 v[220:221], s[40:41], 0, v[168:169]
	s_mov_b32 m0, s29
	s_nop 0
	global_load_lds_dwordx4 v[220:221], off
	s_waitcnt lgkmcnt(0)
	v_mfma_scale_f32_16x16x128_f8f6f4 v[112:115], v[2:7], v[40:45], v[112:115], v187, v187 op_sel_hi:[0,0,0] cbsz:2 blgp:2
	v_mfma_scale_f32_16x16x128_f8f6f4 v[100:103], v[8:13], v[40:45], v[100:103], v187, v187 op_sel_hi:[0,0,0] cbsz:2 blgp:2
	v_mfma_scale_f32_16x16x128_f8f6f4 v[92:95], v[14:19], v[40:45], v[92:95], v187, v187 op_sel_hi:[0,0,0] cbsz:2 blgp:2
	v_mfma_scale_f32_16x16x128_f8f6f4 v[88:91], v[26:31], v[40:45], v[88:91], v187, v187 op_sel_hi:[0,0,0] cbsz:2 blgp:2
	v_mfma_scale_f32_16x16x128_f8f6f4 v[84:87], v[2:7], v[188:193], v[84:87], v187, v187 op_sel_hi:[0,0,0] cbsz:2 blgp:2
	v_mfma_scale_f32_16x16x128_f8f6f4 v[76:79], v[8:13], v[188:193], v[76:79], v187, v187 op_sel_hi:[0,0,0] cbsz:2 blgp:2
	v_mfma_scale_f32_16x16x128_f8f6f4 v[68:71], v[14:19], v[188:193], v[68:71], v187, v187 op_sel_hi:[0,0,0] cbsz:2 blgp:2
	v_mfma_scale_f32_16x16x128_f8f6f4 v[60:63], v[26:31], v[188:193], v[60:63], v187, v187 op_sel_hi:[0,0,0] cbsz:2 blgp:2
	ds_read_b128 v[2:5], v170 offset:12288
	ds_read_b64 v[6:7], v173 offset:12352
	ds_read_b128 v[8:11], v170 offset:13824
	ds_read_b64 v[12:13], v173 offset:13888
	ds_read_b128 v[14:17], v170 offset:15360
	ds_read_b64 v[18:19], v173 offset:15424
	ds_read_b128 v[26:29], v170 offset:16896
	ds_read_b64 v[30:31], v173 offset:16960
	v_mfma_scale_f32_16x16x128_f8f6f4 v[144:147], v[46:51], v[20:25], v[144:147], v187, v187 op_sel_hi:[0,0,0] cbsz:2 blgp:2
	v_mfma_scale_f32_16x16x128_f8f6f4 v[136:139], v[194:199], v[20:25], v[136:139], v187, v187 op_sel_hi:[0,0,0] cbsz:2 blgp:2
	v_mfma_scale_f32_16x16x128_f8f6f4 v[128:131], v[200:205], v[20:25], v[128:131], v187, v187 op_sel_hi:[0,0,0] cbsz:2 blgp:2
	v_mfma_scale_f32_16x16x128_f8f6f4 v[120:123], v[206:211], v[20:25], v[120:123], v187, v187 op_sel_hi:[0,0,0] cbsz:2 blgp:2
	v_mfma_scale_f32_16x16x128_f8f6f4 v[116:119], v[46:51], v[32:37], v[116:119], v187, v187 op_sel_hi:[0,0,0] cbsz:2 blgp:2
	v_mfma_scale_f32_16x16x128_f8f6f4 v[108:111], v[194:199], v[32:37], v[108:111], v187, v187 op_sel_hi:[0,0,0] cbsz:2 blgp:2
	v_mfma_scale_f32_16x16x128_f8f6f4 v[104:107], v[200:205], v[32:37], v[104:107], v187, v187 op_sel_hi:[0,0,0] cbsz:2 blgp:2
	v_mfma_scale_f32_16x16x128_f8f6f4 v[96:99], v[206:211], v[32:37], v[96:99], v187, v187 op_sel_hi:[0,0,0] cbsz:2 blgp:2
	s_add_u32 s38, s2, 0x3000
	s_addc_u32 s39, s3, 0
	s_add_u32 s37, s2, 0x5000
	s_addc_u32 s42, s3, 0
	s_add_u32 s43, s11, 0x2000
	s_addc_u32 s44, s35, 0
	s_and_b64 s[40:41], s[0:1], exec
	s_cselect_b32 s41, s42, s44
	s_cselect_b32 s40, s37, s43
	s_add_u32 s42, s11, 0x4000
	s_addc_u32 s43, s35, 0
	s_mov_b32 m0, s30
	ds_read_b128 v[20:23], v1
	ds_read_b64 v[24:25], v172 offset:64
	ds_read_b128 v[32:35], v1 offset:1536
	ds_read_b64 v[36:37], v172 offset:1600
	s_waitcnt vmcnt(3)
	s_barrier
	s_nop 0
	v_lshl_add_u64 v[220:221], s[38:39], 0, v[168:169]
	global_load_lds_dwordx4 v[220:221], off
	v_lshl_add_u64 v[220:221], s[40:41], 0, v[168:169]
	s_mov_b32 m0, s31
	s_nop 0
	global_load_lds_dwordx4 v[220:221], off
	v_lshl_add_u64 v[220:221], s[42:43], 0, v[168:169]
	s_mov_b32 m0, s33
	s_nop 0
	global_load_lds_dwordx4 v[220:221], off
	v_mfma_scale_f32_16x16x128_f8f6f4 v[80:83], v[46:51], v[40:45], v[80:83], v187, v187 op_sel_hi:[0,0,0] cbsz:2 blgp:2
	v_mfma_scale_f32_16x16x128_f8f6f4 v[72:75], v[194:199], v[40:45], v[72:75], v187, v187 op_sel_hi:[0,0,0] cbsz:2 blgp:2
	v_mfma_scale_f32_16x16x128_f8f6f4 v[64:67], v[200:205], v[40:45], v[64:67], v187, v187 op_sel_hi:[0,0,0] cbsz:2 blgp:2
	v_mfma_scale_f32_16x16x128_f8f6f4 v[56:59], v[206:211], v[40:45], v[56:59], v187, v187 op_sel_hi:[0,0,0] cbsz:2 blgp:2
	v_mfma_scale_f32_16x16x128_f8f6f4 v[52:55], v[46:51], v[188:193], v[52:55], v187, v187 op_sel_hi:[0,0,0] cbsz:2 blgp:2
	v_mfma_scale_f32_16x16x128_f8f6f4 v[48:51], v[194:199], v[188:193], v[224:227], v187, v187 op_sel_hi:[0,0,0] cbsz:2 blgp:2
	v_mfma_scale_f32_16x16x128_f8f6f4 v[44:47], v[200:205], v[188:193], v[212:215], v187, v187 op_sel_hi:[0,0,0] cbsz:2 blgp:2
	v_mfma_scale_f32_16x16x128_f8f6f4 v[40:43], v[206:211], v[188:193], v[216:219], v187, v187 op_sel_hi:[0,0,0] cbsz:2 blgp:2
	s_add_i32 s36, s36, 2
	s_add_u32 s11, s11, 0xc000
	s_addc_u32 s35, s35, 0
	s_add_u32 s2, s2, 0xc000
	s_addc_u32 s3, s3, 0
	s_cmp_lt_u32 s36, 4
	s_waitcnt lgkmcnt(0)
	s_cbranch_scc1 .LBB1_3
	s_mov_b32 s2, 1
	s_cmp_lt_i32 s2, 1
	s_cbranch_scc1 .LBB1_6
.LBB1_5:
	ds_read_b128 v[188:191], v1 offset:24576
	ds_read_b64 v[192:193], v172 offset:24640
	ds_read_b128 v[194:197], v1 offset:26112
	ds_read_b64 v[198:199], v172 offset:26176
	ds_read_b128 v[200:203], v170 offset:36864
	ds_read_b64 v[204:205], v173 offset:36928
	ds_read_b128 v[206:209], v170 offset:38400
	ds_read_b64 v[210:211], v173 offset:38464
	ds_read_b128 v[212:215], v170 offset:39936
	ds_read_b64 v[216:217], v173 offset:40000
	ds_read_b128 v[218:221], v170 offset:41472
	ds_read_b64 v[222:223], v173 offset:41536
	v_mfma_scale_f32_16x16x128_f8f6f4 v[164:167], v[2:7], v[20:25], v[164:167], v187, v187 op_sel_hi:[0,0,0] cbsz:2 blgp:2
	v_mfma_scale_f32_16x16x128_f8f6f4 v[160:163], v[8:13], v[20:25], v[160:163], v187, v187 op_sel_hi:[0,0,0] cbsz:2 blgp:2
	v_mfma_scale_f32_16x16x128_f8f6f4 v[156:159], v[14:19], v[20:25], v[156:159], v187, v187 op_sel_hi:[0,0,0] cbsz:2 blgp:2
	v_mfma_scale_f32_16x16x128_f8f6f4 v[152:155], v[26:31], v[20:25], v[152:155], v187, v187 op_sel_hi:[0,0,0] cbsz:2 blgp:2
	v_mfma_scale_f32_16x16x128_f8f6f4 v[148:151], v[2:7], v[32:37], v[148:151], v187, v187 op_sel_hi:[0,0,0] cbsz:2 blgp:2
	v_mfma_scale_f32_16x16x128_f8f6f4 v[140:143], v[8:13], v[32:37], v[140:143], v187, v187 op_sel_hi:[0,0,0] cbsz:2 blgp:2
	v_mfma_scale_f32_16x16x128_f8f6f4 v[132:135], v[14:19], v[32:37], v[132:135], v187, v187 op_sel_hi:[0,0,0] cbsz:2 blgp:2
	v_mfma_scale_f32_16x16x128_f8f6f4 v[124:127], v[26:31], v[32:37], v[124:127], v187, v187 op_sel_hi:[0,0,0] cbsz:2 blgp:2
	s_waitcnt vmcnt(3)
	s_barrier
	s_waitcnt lgkmcnt(0)
	v_mfma_scale_f32_16x16x128_f8f6f4 v[112:115], v[2:7], v[188:193], v[112:115], v187, v187 op_sel_hi:[0,0,0] cbsz:2 blgp:2
	v_mfma_scale_f32_16x16x128_f8f6f4 v[100:103], v[8:13], v[188:193], v[100:103], v187, v187 op_sel_hi:[0,0,0] cbsz:2 blgp:2
	v_mfma_scale_f32_16x16x128_f8f6f4 v[92:95], v[14:19], v[188:193], v[92:95], v187, v187 op_sel_hi:[0,0,0] cbsz:2 blgp:2
	v_mfma_scale_f32_16x16x128_f8f6f4 v[88:91], v[26:31], v[188:193], v[88:91], v187, v187 op_sel_hi:[0,0,0] cbsz:2 blgp:2
	v_mfma_scale_f32_16x16x128_f8f6f4 v[84:87], v[2:7], v[194:199], v[84:87], v187, v187 op_sel_hi:[0,0,0] cbsz:2 blgp:2
	v_mfma_scale_f32_16x16x128_f8f6f4 v[76:79], v[8:13], v[194:199], v[76:79], v187, v187 op_sel_hi:[0,0,0] cbsz:2 blgp:2
	v_mfma_scale_f32_16x16x128_f8f6f4 v[68:71], v[14:19], v[194:199], v[68:71], v187, v187 op_sel_hi:[0,0,0] cbsz:2 blgp:2
	v_mfma_scale_f32_16x16x128_f8f6f4 v[60:63], v[26:31], v[194:199], v[60:63], v187, v187 op_sel_hi:[0,0,0] cbsz:2 blgp:2
	ds_read_b128 v[2:5], v170 offset:61440
	ds_read_b64 v[6:7], v173 offset:61504
	ds_read_b128 v[8:11], v170 offset:62976
	ds_read_b64 v[12:13], v173 offset:63040
	ds_read_b128 v[14:17], v170 offset:64512
	ds_read_b64 v[18:19], v173 offset:64576
	ds_read_b128 v[26:29], v171 offset:53760
	ds_read_b64 v[30:31], v174 offset:53760
	v_mfma_scale_f32_16x16x128_f8f6f4 v[144:147], v[200:205], v[20:25], v[144:147], v187, v187 op_sel_hi:[0,0,0] cbsz:2 blgp:2
	v_mfma_scale_f32_16x16x128_f8f6f4 v[136:139], v[206:211], v[20:25], v[136:139], v187, v187 op_sel_hi:[0,0,0] cbsz:2 blgp:2
	v_mfma_scale_f32_16x16x128_f8f6f4 v[128:131], v[212:217], v[20:25], v[128:131], v187, v187 op_sel_hi:[0,0,0] cbsz:2 blgp:2
	v_mfma_scale_f32_16x16x128_f8f6f4 v[120:123], v[218:223], v[20:25], v[120:123], v187, v187 op_sel_hi:[0,0,0] cbsz:2 blgp:2
	v_mfma_scale_f32_16x16x128_f8f6f4 v[116:119], v[200:205], v[32:37], v[116:119], v187, v187 op_sel_hi:[0,0,0] cbsz:2 blgp:2
	v_mfma_scale_f32_16x16x128_f8f6f4 v[108:111], v[206:211], v[32:37], v[108:111], v187, v187 op_sel_hi:[0,0,0] cbsz:2 blgp:2
	v_mfma_scale_f32_16x16x128_f8f6f4 v[104:107], v[212:217], v[32:37], v[104:107], v187, v187 op_sel_hi:[0,0,0] cbsz:2 blgp:2
	v_mfma_scale_f32_16x16x128_f8f6f4 v[96:99], v[218:223], v[32:37], v[96:99], v187, v187 op_sel_hi:[0,0,0] cbsz:2 blgp:2
	ds_read_b128 v[20:23], v1 offset:49152
	ds_read_b64 v[24:25], v172 offset:49216
	ds_read_b128 v[32:35], v1 offset:50688
	ds_read_b64 v[36:37], v172 offset:50752
	s_waitcnt vmcnt(0)
	s_barrier
	v_mfma_scale_f32_16x16x128_f8f6f4 v[80:83], v[200:205], v[188:193], v[80:83], v187, v187 op_sel_hi:[0,0,0] cbsz:2 blgp:2
	v_mfma_scale_f32_16x16x128_f8f6f4 v[72:75], v[206:211], v[188:193], v[72:75], v187, v187 op_sel_hi:[0,0,0] cbsz:2 blgp:2
	v_mfma_scale_f32_16x16x128_f8f6f4 v[64:67], v[212:217], v[188:193], v[64:67], v187, v187 op_sel_hi:[0,0,0] cbsz:2 blgp:2
	v_mfma_scale_f32_16x16x128_f8f6f4 v[56:59], v[218:223], v[188:193], v[56:59], v187, v187 op_sel_hi:[0,0,0] cbsz:2 blgp:2
	v_mfma_scale_f32_16x16x128_f8f6f4 v[52:55], v[200:205], v[194:199], v[52:55], v187, v187 op_sel_hi:[0,0,0] cbsz:2 blgp:2
	v_mfma_scale_f32_16x16x128_f8f6f4 v[224:227], v[206:211], v[194:199], v[48:51], v187, v187 op_sel_hi:[0,0,0] cbsz:2 blgp:2
	v_mfma_scale_f32_16x16x128_f8f6f4 v[212:215], v[212:217], v[194:199], v[44:47], v187, v187 op_sel_hi:[0,0,0] cbsz:2 blgp:2
	v_mfma_scale_f32_16x16x128_f8f6f4 v[216:219], v[218:223], v[194:199], v[40:43], v187, v187 op_sel_hi:[0,0,0] cbsz:2 blgp:2
	s_waitcnt lgkmcnt(0)
	s_nop 0
	ds_read_b128 v[40:43], v175
	ds_read_b64 v[44:45], v176
	ds_read_b128 v[188:191], v179
	ds_read_b64 v[192:193], v180
	ds_read_b128 v[46:49], v177
	ds_read_b64 v[50:51], v178
	ds_read_b128 v[194:197], v181
	ds_read_b64 v[198:199], v182
	ds_read_b128 v[200:203], v183
	ds_read_b64 v[204:205], v184
	ds_read_b128 v[206:209], v185
	ds_read_b64 v[210:211], v186
	v_mfma_scale_f32_16x16x128_f8f6f4 v[164:167], v[2:7], v[20:25], v[164:167], v187, v187 op_sel_hi:[0,0,0] cbsz:2 blgp:2
	v_mfma_scale_f32_16x16x128_f8f6f4 v[160:163], v[8:13], v[20:25], v[160:163], v187, v187 op_sel_hi:[0,0,0] cbsz:2 blgp:2
	v_mfma_scale_f32_16x16x128_f8f6f4 v[156:159], v[14:19], v[20:25], v[156:159], v187, v187 op_sel_hi:[0,0,0] cbsz:2 blgp:2
	v_mfma_scale_f32_16x16x128_f8f6f4 v[152:155], v[26:31], v[20:25], v[152:155], v187, v187 op_sel_hi:[0,0,0] cbsz:2 blgp:2
	v_mfma_scale_f32_16x16x128_f8f6f4 v[148:151], v[2:7], v[32:37], v[148:151], v187, v187 op_sel_hi:[0,0,0] cbsz:2 blgp:2
	v_mfma_scale_f32_16x16x128_f8f6f4 v[140:143], v[8:13], v[32:37], v[140:143], v187, v187 op_sel_hi:[0,0,0] cbsz:2 blgp:2
	v_mfma_scale_f32_16x16x128_f8f6f4 v[132:135], v[14:19], v[32:37], v[132:135], v187, v187 op_sel_hi:[0,0,0] cbsz:2 blgp:2
	v_mfma_scale_f32_16x16x128_f8f6f4 v[124:127], v[26:31], v[32:37], v[124:127], v187, v187 op_sel_hi:[0,0,0] cbsz:2 blgp:2
	s_waitcnt lgkmcnt(0)
	v_mfma_scale_f32_16x16x128_f8f6f4 v[112:115], v[2:7], v[40:45], v[112:115], v187, v187 op_sel_hi:[0,0,0] cbsz:2 blgp:2
	v_mfma_scale_f32_16x16x128_f8f6f4 v[100:103], v[8:13], v[40:45], v[100:103], v187, v187 op_sel_hi:[0,0,0] cbsz:2 blgp:2
	v_mfma_scale_f32_16x16x128_f8f6f4 v[92:95], v[14:19], v[40:45], v[92:95], v187, v187 op_sel_hi:[0,0,0] cbsz:2 blgp:2
	v_mfma_scale_f32_16x16x128_f8f6f4 v[88:91], v[26:31], v[40:45], v[88:91], v187, v187 op_sel_hi:[0,0,0] cbsz:2 blgp:2
	v_mfma_scale_f32_16x16x128_f8f6f4 v[84:87], v[2:7], v[188:193], v[84:87], v187, v187 op_sel_hi:[0,0,0] cbsz:2 blgp:2
	v_mfma_scale_f32_16x16x128_f8f6f4 v[76:79], v[8:13], v[188:193], v[76:79], v187, v187 op_sel_hi:[0,0,0] cbsz:2 blgp:2
	v_mfma_scale_f32_16x16x128_f8f6f4 v[68:71], v[14:19], v[188:193], v[68:71], v187, v187 op_sel_hi:[0,0,0] cbsz:2 blgp:2
	v_mfma_scale_f32_16x16x128_f8f6f4 v[60:63], v[26:31], v[188:193], v[60:63], v187, v187 op_sel_hi:[0,0,0] cbsz:2 blgp:2
	v_mfma_scale_f32_16x16x128_f8f6f4 v[144:147], v[46:51], v[20:25], v[144:147], v187, v187 op_sel_hi:[0,0,0] cbsz:2 blgp:2
	v_mfma_scale_f32_16x16x128_f8f6f4 v[136:139], v[194:199], v[20:25], v[136:139], v187, v187 op_sel_hi:[0,0,0] cbsz:2 blgp:2
	v_mfma_scale_f32_16x16x128_f8f6f4 v[128:131], v[200:205], v[20:25], v[128:131], v187, v187 op_sel_hi:[0,0,0] cbsz:2 blgp:2
	v_mfma_scale_f32_16x16x128_f8f6f4 v[120:123], v[206:211], v[20:25], v[120:123], v187, v187 op_sel_hi:[0,0,0] cbsz:2 blgp:2
	v_mfma_scale_f32_16x16x128_f8f6f4 v[116:119], v[46:51], v[32:37], v[116:119], v187, v187 op_sel_hi:[0,0,0] cbsz:2 blgp:2
	v_mfma_scale_f32_16x16x128_f8f6f4 v[108:111], v[194:199], v[32:37], v[108:111], v187, v187 op_sel_hi:[0,0,0] cbsz:2 blgp:2
	v_mfma_scale_f32_16x16x128_f8f6f4 v[104:107], v[200:205], v[32:37], v[104:107], v187, v187 op_sel_hi:[0,0,0] cbsz:2 blgp:2
	v_mfma_scale_f32_16x16x128_f8f6f4 v[96:99], v[206:211], v[32:37], v[96:99], v187, v187 op_sel_hi:[0,0,0] cbsz:2 blgp:2
	v_mfma_scale_f32_16x16x128_f8f6f4 v[80:83], v[46:51], v[40:45], v[80:83], v187, v187 op_sel_hi:[0,0,0] cbsz:2 blgp:2
	v_mfma_scale_f32_16x16x128_f8f6f4 v[72:75], v[194:199], v[40:45], v[72:75], v187, v187 op_sel_hi:[0,0,0] cbsz:2 blgp:2
	v_mfma_scale_f32_16x16x128_f8f6f4 v[64:67], v[200:205], v[40:45], v[64:67], v187, v187 op_sel_hi:[0,0,0] cbsz:2 blgp:2
	v_mfma_scale_f32_16x16x128_f8f6f4 v[56:59], v[206:211], v[40:45], v[56:59], v187, v187 op_sel_hi:[0,0,0] cbsz:2 blgp:2
	v_mfma_scale_f32_16x16x128_f8f6f4 v[52:55], v[46:51], v[188:193], v[52:55], v187, v187 op_sel_hi:[0,0,0] cbsz:2 blgp:2
	v_mfma_scale_f32_16x16x128_f8f6f4 v[48:51], v[194:199], v[188:193], v[224:227], v187, v187 op_sel_hi:[0,0,0] cbsz:2 blgp:2
	v_mfma_scale_f32_16x16x128_f8f6f4 v[44:47], v[200:205], v[188:193], v[212:215], v187, v187 op_sel_hi:[0,0,0] cbsz:2 blgp:2
	v_mfma_scale_f32_16x16x128_f8f6f4 v[40:43], v[206:211], v[188:193], v[216:219], v187, v187 op_sel_hi:[0,0,0] cbsz:2 blgp:2
	s_add_i32 s2, s2, -1
	s_cmp_lg_u32 s2, 0
	s_cbranch_scc1 .LBB1_5
